# stack: MoE A-pairing + B two sets; A-pairing in phases 2/6; phase-6 epilogue pipelined; phase-4 loop pipelined; phase-10 ln2 g/b hoisted
# baseline (speedup 1.0000x reference)
.LBB0_1394:
	s_cmp_lt_i32 s30, 11
	s_cselect_b64 s[0:1], -1, 0
	s_and_b64 s[0:1], s[0:1], s[4:5]
	s_andn2_b64 vcc, exec, s[0:1]
	s_cbranch_vccnz .LBB0_1398
	s_waitcnt vmcnt(16)
	v_lshl_or_b32 v32, s88, 3, v222
	s_movk_i32 s7, 0x2000
	v_cmp_gt_i32_e32 vcc, s7, v32
	s_and_saveexec_b64 s[0:1], vcc
	s_cbranch_execz .LBB0_1398
	s_waitcnt vmcnt(0)
	v_and_b32_e32 v3, 63, v0
	v_lshlrev_b32_e32 v34, 4, v3
	v_mov_b32_e32 v35, 0
	v_lshl_add_u64 v[0:1], s[28:29], 0, v[34:35]
	s_mov_b64 s[0:1], 0xb000000
	v_lshl_add_u64 v[36:37], v[0:1], 0, s[0:1]
	v_mbcnt_lo_u32_b32 v0, -1, 0
	v_mbcnt_hi_u32_b32 v0, -1, v0
	v_and_b32_e32 v1, 64, v0
	v_add_u32_e32 v1, 64, v1
	v_xor_b32_e32 v2, 1, v0
	v_cmp_lt_i32_e32 vcc, v2, v1
	s_load_dword s0, s[90:91], 0x110
	v_lshl_add_u64 v[38:39], s[42:43], 0, v[34:35]
	v_cndmask_b32_e32 v2, v0, v2, vcc
	v_lshlrev_b32_e32 v136, 2, v2
	v_xor_b32_e32 v2, 2, v0
	v_cmp_lt_i32_e32 vcc, v2, v1
	v_lshl_add_u64 v[40:41], s[44:45], 0, v[34:35]
	v_mov_b32_e32 v17, v35
	v_cndmask_b32_e32 v2, v0, v2, vcc
	v_lshlrev_b32_e32 v137, 2, v2
	v_xor_b32_e32 v2, 4, v0
	v_cmp_lt_i32_e32 vcc, v2, v1
	s_waitcnt lgkmcnt(0)
	v_lshl_add_u64 v[58:59], s[22:23], 0, v[34:35]
	v_lshl_add_u64 v[60:61], s[24:25], 0, v[34:35]
	v_cndmask_b32_e32 v2, v0, v2, vcc
	v_lshlrev_b32_e32 v138, 2, v2
	v_xor_b32_e32 v2, 8, v0
	v_cmp_lt_i32_e32 vcc, v2, v1
	v_lshlrev_b32_e32 v34, 3, v3
	s_lshl_b32 s8, s0, 3
	v_cndmask_b32_e32 v2, v0, v2, vcc
	v_lshlrev_b32_e32 v139, 2, v2
	v_xor_b32_e32 v2, 16, v0
	v_cmp_lt_i32_e32 vcc, v2, v1
	v_mov_b32_e32 v19, v35
	v_mov_b32_e32 v21, v35
	v_cndmask_b32_e32 v2, v0, v2, vcc
	v_lshlrev_b32_e32 v140, 2, v2
	v_xor_b32_e32 v2, 32, v0
	v_cmp_lt_i32_e32 vcc, v2, v1
	v_mov_b32_e32 v23, v35
	s_mov_b64 s[0:1], 0x1d600000
	v_cndmask_b32_e32 v0, v0, v2, vcc
	v_lshlrev_b32_e32 v141, 2, v0
	v_lshlrev_b32_e32 v0, 2, v3
	v_or_b32_e32 v8, 0x400, v0
	v_or_b32_e32 v10, 0x500, v0
	v_or_b32_e32 v12, 0x600, v0
	v_or_b32_e32 v14, 0x700, v0
	v_lshlrev_b32_e32 v16, 2, v8
	v_or_b32_e32 v2, 0x100, v0
	v_or_b32_e32 v4, 0x200, v0
	v_or_b32_e32 v6, 0x300, v0
	v_lshl_add_u64 v[42:43], s[42:43], 0, v[16:17]
	v_lshl_add_u64 v[44:45], s[44:45], 0, v[16:17]
	v_lshlrev_b32_e32 v18, 2, v10
	v_lshlrev_b32_e32 v20, 2, v12
	v_lshlrev_b32_e32 v22, 2, v14
	v_lshl_add_u64 v[62:63], s[22:23], 0, v[16:17]
	v_lshl_add_u64 v[64:65], s[24:25], 0, v[16:17]
	v_lshl_add_u64 v[16:17], s[28:29], 0, v[34:35]
	v_lshl_add_u64 v[46:47], s[42:43], 0, v[18:19]
	v_lshl_add_u64 v[48:49], s[44:45], 0, v[18:19]
	v_lshl_add_u64 v[50:51], s[42:43], 0, v[20:21]
	v_lshl_add_u64 v[52:53], s[44:45], 0, v[20:21]
	v_lshl_add_u64 v[54:55], s[42:43], 0, v[22:23]
	v_lshl_add_u64 v[56:57], s[44:45], 0, v[22:23]
	v_lshl_add_u64 v[66:67], s[22:23], 0, v[18:19]
	v_lshl_add_u64 v[68:69], s[24:25], 0, v[18:19]
	v_lshl_add_u64 v[70:71], s[22:23], 0, v[20:21]
	v_lshl_add_u64 v[72:73], s[24:25], 0, v[20:21]
	v_lshl_add_u64 v[74:75], s[22:23], 0, v[22:23]
	v_lshl_add_u64 v[76:77], s[24:25], 0, v[22:23]
	v_lshl_add_u64 v[78:79], v[16:17], 0, s[0:1]
	s_mov_b64 s[2:3], 0
	s_movk_i32 s9, 0x1000
	v_mov_b32_e32 v142, 0x3727c5ac
	s_mov_b32 s10, 0xf800000
	v_mov_b32_e32 v143, 0x260
	s_movk_i32 s11, 0x3000
	s_mov_b64 s[4:5], 0x20a000
	v_lshlrev_b32_e32 v34, 2, v0
	s_mov_b32 s6, 0x3f9837f0
	v_lshlrev_b32_e32 v80, 2, v2
	v_lshlrev_b32_e32 v82, 2, v4
	v_lshlrev_b32_e32 v84, 2, v6
	v_lshlrev_b32_e32 v86, 2, v8
	v_lshlrev_b32_e32 v88, 2, v10
	v_lshlrev_b32_e32 v90, 2, v12
	v_lshlrev_b32_e32 v92, 2, v14
	s_movk_i32 s12, 0x1fff
	global_load_dwordx4 v[198:201], v[58:59], off offset:1024
	global_load_dwordx4 v[202:205], v[60:61], off offset:1024
	global_load_dwordx4 v[206:209], v[58:59], off offset:2048
	global_load_dwordx4 v[210:213], v[60:61], off offset:2048
	global_load_dwordx4 v[214:217], v[58:59], off offset:3072
	global_load_dwordx4 v[218:221], v[60:61], off offset:3072
	global_load_dwordx4 v[224:227], v[62:63], off
	global_load_dwordx4 v[228:231], v[64:65], off
	global_load_dwordx4 v[232:235], v[66:67], off
	global_load_dwordx4 v[236:239], v[68:69], off
	global_load_dwordx4 v[240:243], v[70:71], off
	global_load_dwordx4 v[244:247], v[72:73], off
	global_load_dwordx4 v[248:251], v[74:75], off
.LBB0_1397:
	v_ashrrev_i32_e32 v33, 31, v32
	v_lshlrev_b64 v[94:95], 13, v[32:33]
	v_lshl_add_u64 v[0:1], v[36:37], 0, v[94:95]
	global_load_dwordx4 v[28:31], v[0:1], off
	global_load_dwordx4 v[24:27], v[0:1], off offset:1024
	global_load_dwordx4 v[20:23], v[0:1], off offset:2048
	global_load_dwordx4 v[4:7], v[0:1], off offset:3072
	v_add_co_u32_e32 v96, vcc, s9, v0
	v_mov_b32_e32 v91, v35
	s_nop 0
	v_addc_co_u32_e32 v97, vcc, 0, v1, vcc
	global_load_dwordx4 v[8:11], v[96:97], off
	global_load_dwordx4 v[12:15], v[96:97], off offset:1024
	global_load_dwordx4 v[16:19], v[96:97], off offset:2048
	global_load_dwordx4 v[0:3], v[96:97], off offset:3072
	v_mov_b32_e32 v93, v35
	s_waitcnt vmcnt(7)
	v_mov_b32_e32 v96, v28
	s_waitcnt vmcnt(6)
	v_mov_b32_e32 v97, v24
	v_mov_b32_e32 v98, v29
	v_mov_b32_e32 v99, v25
	v_mov_b32_e32 v100, v30
	v_mov_b32_e32 v101, v26
	v_mov_b32_e32 v102, v31
	v_mov_b32_e32 v103, v27
	s_waitcnt vmcnt(5)
	v_mov_b32_e32 v104, v21
	v_mov_b32_e32 v105, v22
	v_mov_b32_e32 v106, v20
	v_mov_b32_e32 v107, v23
	v_pk_add_f32 v[96:97], v[96:97], v[98:99]
	v_pk_add_f32 v[98:99], v[100:101], v[102:103]
	v_pk_add_f32 v[100:101], v[104:105], v[106:107]
	v_pk_add_f32 v[96:97], v[96:97], v[98:99]
	v_pk_add_f32 v[98:99], v[100:101], v[100:101] op_sel:[0,1] op_sel_hi:[1,0]
	v_add_f32_e32 v81, 0, v96
	s_waitcnt vmcnt(4)
	v_add_f32_e32 v108, v4, v5
	v_add_f32_e32 v110, v6, v7
	s_waitcnt vmcnt(3)
	v_mov_b32_e32 v103, v8
	v_mov_b32_e32 v109, v10
	v_mov_b32_e32 v111, v11
	v_mov_b32_e32 v99, v9
	v_add_f32_e32 v102, v81, v97
	s_waitcnt vmcnt(2)
	v_mov_b32_e32 v104, v13
	v_mov_b32_e32 v105, v14
	v_mov_b32_e32 v106, v12
	v_mov_b32_e32 v107, v15
	v_pk_add_f32 v[100:101], v[108:109], v[110:111]
	v_pk_add_f32 v[96:97], v[102:103], v[98:99]
	v_pk_add_f32 v[104:105], v[104:105], v[106:107]
	v_pk_add_f32 v[96:97], v[96:97], v[100:101]
	v_pk_add_f32 v[104:105], v[104:105], v[104:105] op_sel:[0,1] op_sel_hi:[1,0]
	v_pk_add_f32 v[96:97], v[96:97], v[96:97] op_sel:[0,1] op_sel_hi:[1,0]
	s_waitcnt vmcnt(1)
	v_add_f32_e32 v112, v16, v17
	v_add_f32_e32 v114, v18, v19
	s_waitcnt vmcnt(0)
	v_mov_b32_e32 v113, v2
	v_mov_b32_e32 v115, v3
	v_mov_b32_e32 v105, v1
	v_mov_b32_e32 v97, v0
	v_pk_add_f32 v[106:107], v[112:113], v[114:115]
	v_pk_add_f32 v[96:97], v[96:97], v[104:105]
	s_nop 0
	v_pk_add_f32 v[96:97], v[96:97], v[106:107]
	s_nop 0
	v_add_f32_e32 v81, v96, v97
	ds_bpermute_b32 v83, v136, v81
	s_waitcnt lgkmcnt(0)
	v_add_f32_e32 v81, v81, v83
	ds_bpermute_b32 v83, v137, v81
	s_waitcnt lgkmcnt(0)
	v_add_f32_e32 v81, v81, v83
	ds_bpermute_b32 v83, v138, v81
	s_waitcnt lgkmcnt(0)
	v_add_f32_e32 v81, v81, v83
	ds_bpermute_b32 v83, v139, v81
	s_waitcnt lgkmcnt(0)
	v_add_f32_e32 v81, v81, v83
	ds_bpermute_b32 v83, v140, v81
	s_waitcnt lgkmcnt(0)
	v_add_f32_e32 v81, v81, v83
	ds_bpermute_b32 v83, v141, v81
	s_waitcnt lgkmcnt(0)
	v_add_f32_e32 v81, v81, v83
	v_fmamk_f32 v99, v81, 0xba000000, v31
	v_fmamk_f32 v29, v81, 0xba000000, v29
	v_fmamk_f32 v101, v81, 0xba000000, v27
	v_fmamk_f32 v25, v81, 0xba000000, v25
	v_fmamk_f32 v98, v81, 0xba000000, v30
	v_fmac_f32_e32 v28, 0xba000000, v81
	v_fmamk_f32 v100, v81, 0xba000000, v26
	v_fmac_f32_e32 v24, 0xba000000, v81
	v_fmamk_f32 v97, v81, 0xba000000, v21
	v_fmamk_f32 v96, v81, 0xba000000, v20
	v_fmamk_f32 v23, v81, 0xba000000, v23
	v_fmac_f32_e32 v22, 0xba000000, v81
	v_fmamk_f32 v117, v81, 0xba000000, v11
	v_fmamk_f32 v116, v81, 0xba000000, v10
	v_mov_b32_e32 v10, v29
	v_mov_b32_e32 v11, v25
	v_mov_b32_e32 v20, v99
	v_mov_b32_e32 v21, v101
	v_fmamk_f32 v31, v81, 0xba000000, v5
	v_fmamk_f32 v30, v81, 0xba000000, v4
	v_fmamk_f32 v121, v81, 0xba000000, v17
	v_fmamk_f32 v120, v81, 0xba000000, v16
	v_mov_b32_e32 v4, v28
	v_mov_b32_e32 v5, v24
	v_mov_b32_e32 v16, v98
	v_mov_b32_e32 v17, v100
	v_pk_mul_f32 v[26:27], v[22:23], v[22:23]
	v_pk_mul_f32 v[102:103], v[96:97], v[96:97]
	v_pk_mul_f32 v[10:11], v[10:11], v[10:11]
	v_pk_mul_f32 v[20:21], v[20:21], v[20:21]
	v_fmac_f32_e32 v6, 0xba000000, v81
	v_pk_mov_b32 v[118:119], v[102:103], v[26:27] op_sel:[1,0]
	v_mov_b32_e32 v103, v27
	v_pk_fma_f32 v[4:5], v[4:5], v[4:5], v[10:11]
	v_pk_fma_f32 v[10:11], v[16:17], v[16:17], v[20:21]
	v_fmamk_f32 v7, v81, 0xba000000, v7
	v_mul_f32_e32 v104, v30, v30
	v_mul_f32_e32 v106, v6, v6
	v_pk_add_f32 v[16:17], v[118:119], v[102:103]
	v_pk_add_f32 v[4:5], v[4:5], v[10:11]
	v_fmamk_f32 v9, v81, 0xba000000, v9
	v_fmac_f32_e32 v8, 0xba000000, v81
	v_fmamk_f32 v13, v81, 0xba000000, v13
	v_fmamk_f32 v12, v81, 0xba000000, v12
	v_fmamk_f32 v15, v81, 0xba000000, v15
	v_fmac_f32_e32 v14, 0xba000000, v81
	v_pk_fma_f32 v[26:27], v[30:31], v[30:31], v[104:105] op_sel_hi:[1,1,0]
	v_pk_fma_f32 v[104:105], v[6:7], v[6:7], v[106:107] op_sel_hi:[1,1,0]
	v_pk_add_f32 v[10:11], v[16:17], v[16:17] op_sel_hi:[0,1]
	v_pk_add_f32 v[4:5], v[4:5], v[4:5] op_sel_hi:[0,1]
	v_pk_mul_f32 v[108:109], v[14:15], v[14:15]
	v_pk_mul_f32 v[110:111], v[12:13], v[12:13]
	v_mul_f32_e32 v26, v8, v8
	v_mul_f32_e32 v104, v9, v9
	v_mul_f32_e32 v10, v116, v116
	v_mul_f32_e32 v4, v117, v117
	v_fmac_f32_e32 v18, 0xba000000, v81
	v_pk_mov_b32 v[106:107], v[110:111], v[108:109] op_sel:[1,0]
	v_mov_b32_e32 v111, v109
	v_pk_add_f32 v[16:17], v[26:27], v[104:105]
	v_pk_add_f32 v[4:5], v[10:11], v[4:5]
	v_fmamk_f32 v19, v81, 0xba000000, v19
	v_mul_f32_e32 v112, v120, v120
	v_mul_f32_e32 v114, v18, v18
	v_pk_add_f32 v[20:21], v[106:107], v[110:111]
	v_pk_add_f32 v[4:5], v[16:17], v[4:5]
	v_pk_fma_f32 v[108:109], v[120:121], v[120:121], v[112:113] op_sel_hi:[1,1,0]
	v_pk_add_f32 v[20:21], v[20:21], v[20:21] op_sel_hi:[0,1]
	v_pk_add_f32 v[4:5], v[4:5], v[4:5] op_sel_hi:[0,1]
	v_pk_fma_f32 v[10:11], v[18:19], v[18:19], v[114:115] op_sel_hi:[1,1,0]
	v_fmamk_f32 v123, v81, 0xba000000, v3
	v_fmamk_f32 v122, v81, 0xba000000, v2
	v_fmamk_f32 v1, v81, 0xba000000, v1
	v_fmac_f32_e32 v0, 0xba000000, v81
	v_mul_f32_e32 v108, v0, v0
	v_mul_f32_e32 v10, v1, v1
	v_mul_f32_e32 v20, v122, v122
	v_mul_f32_e32 v4, v123, v123
	v_pk_add_f32 v[2:3], v[108:109], v[10:11]
	v_pk_add_f32 v[4:5], v[20:21], v[4:5]
	s_nop 0
	v_pk_add_f32 v[2:3], v[2:3], v[4:5]
	s_nop 0
	v_add_f32_e32 v2, v2, v3
	ds_bpermute_b32 v3, v136, v2
	s_waitcnt lgkmcnt(0)
	v_add_f32_e32 v10, v2, v3
	ds_bpermute_b32 v11, v137, v10
	global_load_dwordx4 v[2:5], v[38:39], off
	global_load_dwordx4 v[102:105], v[40:41], off
	global_load_dwordx4 v[132:135], v[38:39], off offset:1024
	global_load_dwordx4 v[144:147], v[40:41], off offset:1024
	global_load_dwordx4 v[148:151], v[40:41], off offset:2048
	global_load_dwordx4 v[152:155], v[38:39], off offset:2048
	global_load_dwordx4 v[156:159], v[38:39], off offset:3072
	global_load_dwordx4 v[160:163], v[40:41], off offset:3072
	global_load_dwordx4 v[164:167], v[42:43], off
	global_load_dwordx4 v[168:171], v[44:45], off
	global_load_dwordx4 v[172:175], v[46:47], off
	s_waitcnt lgkmcnt(0)
	v_add_f32_e32 v10, v10, v11
	ds_bpermute_b32 v11, v138, v10
	global_load_dwordx4 v[176:179], v[48:49], off
	global_load_dwordx4 v[180:183], v[50:51], off
	global_load_dwordx4 v[184:187], v[52:53], off
	global_load_dwordx4 v[188:191], v[54:55], off
	global_load_dwordx4 v[192:195], v[56:57], off
	s_waitcnt lgkmcnt(0)
	v_add_f32_e32 v10, v10, v11
	ds_bpermute_b32 v11, v139, v10
	s_waitcnt lgkmcnt(0)
	v_add_f32_e32 v10, v10, v11
	ds_bpermute_b32 v11, v140, v10
	s_waitcnt lgkmcnt(0)
	v_add_f32_e32 v10, v10, v11
	ds_bpermute_b32 v11, v141, v10
	s_waitcnt lgkmcnt(0)
	v_add_f32_e32 v10, v10, v11
	v_fmamk_f32 v10, v10, 0x3a000000, v142
	v_mul_f32_e32 v11, 0x4f800000, v10
	v_cmp_gt_f32_e32 vcc, s10, v10
	s_nop 1
	v_cndmask_b32_e32 v16, v10, v11, vcc
	v_sqrt_f32_e32 v10, v16
	s_nop 0
	v_add_u32_e32 v11, -1, v10
	v_add_u32_e32 v17, 1, v10
	v_fma_f32 v20, -v11, v10, v16
	v_fma_f32 v21, -v17, v10, v16
	v_cmp_ge_f32_e64 s[0:1], 0, v20
	s_nop 1
	v_cndmask_b32_e64 v10, v10, v11, s[0:1]
	v_cmp_lt_f32_e64 s[0:1], 0, v21
	s_nop 1
	v_cndmask_b32_e64 v17, v10, v17, s[0:1]
	v_lshlrev_b64 v[10:11], 14, v[32:33]
	v_lshl_add_u64 v[26:27], v[78:79], 0, v[10:11]
	v_mul_f32_e32 v20, 0x37800000, v17
	global_load_dwordx2 v[126:127], v[26:27], off
	v_cndmask_b32_e32 v10, v17, v20, vcc
	v_cmp_class_f32_e32 vcc, v16, v143
	global_load_dwordx2 v[114:115], v[26:27], off offset:512
	s_nop 0
	v_cndmask_b32_e32 v16, v10, v16, vcc
	v_add_co_u32_e32 v10, vcc, s7, v26
	v_div_scale_f32 v17, s[0:1], v16, v16, 1.0
	s_nop 0
	v_addc_co_u32_e32 v11, vcc, 0, v27, vcc
	global_load_dwordx2 v[130:131], v[10:11], off offset:-4096
	v_rcp_f32_e32 v20, v17
	global_load_dwordx2 v[196:197], v[10:11], off
	v_fma_f32 v21, -v17, v20, 1.0
	v_fmac_f32_e32 v20, v21, v20
	v_div_scale_f32 v21, vcc, 1.0, v16, 1.0
	v_mul_f32_e32 v81, v21, v20
	v_fma_f32 v83, -v17, v81, v21
	v_fmac_f32_e32 v81, v83, v20
	v_fma_f32 v17, -v17, v81, v21
	v_div_fmas_f32 v17, v17, v20, v81
	v_div_fixup_f32 v124, v17, v16, 1.0
	v_pk_mul_f32 v[20:21], v[28:29], v[124:125] op_sel_hi:[1,0]
	v_pk_mul_f32 v[16:17], v[98:99], v[124:125] op_sel_hi:[1,0]
	s_waitcnt vmcnt(18)
	v_pk_fma_f32 v[108:109], v[2:3], v[20:21], v[102:103]
	v_pk_mul_f32 v[2:3], v[24:25], v[124:125] op_sel_hi:[1,0]
	v_add_co_u32_e32 v20, vcc, s11, v26
	v_pk_fma_f32 v[110:111], v[4:5], v[16:17], v[104:105]
	s_nop 0
	v_addc_co_u32_e32 v21, vcc, 0, v27, vcc
	s_waitcnt vmcnt(16)
	v_pk_fma_f32 v[104:105], v[132:133], v[2:3], v[144:145]
	v_lshrrev_b32_e32 v2, 20, v33
	global_load_dwordx2 v[112:113], v[20:21], off
	v_add_u32_e32 v2, v32, v2
	v_ashrrev_i32_e32 v2, 12, v2
	v_mul_i32_i24_e32 v2, 0x3000, v2
	v_ashrrev_i32_e32 v3, 31, v2
	v_pk_mul_f32 v[6:7], v[6:7], v[124:125] op_sel_hi:[1,0]
	v_lshl_add_u64 v[2:3], v[2:3], 2, s[28:29]
	s_waitcnt vmcnt(13)
	v_pk_fma_f32 v[98:99], v[158:159], v[6:7], v[162:163]
	v_pk_mul_f32 v[6:7], v[116:117], v[124:125] op_sel_hi:[1,0]
	v_add_co_u32_e32 v116, vcc, s9, v26
	v_lshl_add_u64 v[16:17], v[2:3], 0, s[4:5]
	s_nop 0
	v_addc_co_u32_e32 v117, vcc, 0, v27, vcc
	v_lshl_add_u64 v[2:3], v[16:17], 0, v[34:35]
	global_load_dwordx2 v[118:119], v[116:117], off offset:512
	v_pk_mul_f32 v[28:29], v[100:101], v[124:125] op_sel_hi:[1,0]
	global_load_dwordx4 v[2:5], v[2:3], off
	v_pk_mul_f32 v[22:23], v[22:23], v[124:125] op_sel_hi:[1,0]
	v_pk_mul_f32 v[8:9], v[8:9], v[124:125] op_sel_hi:[1,0]
	v_pk_fma_f32 v[106:107], v[134:135], v[28:29], v[146:147]
	v_pk_mul_f32 v[24:25], v[96:97], v[124:125] op_sel_hi:[1,0]
	v_pk_fma_f32 v[102:103], v[154:155], v[22:23], v[150:151]
	v_pk_mul_f32 v[22:23], v[30:31], v[124:125] op_sel_hi:[1,0]
	s_waitcnt vmcnt(13)
	v_pk_fma_f32 v[28:29], v[164:165], v[8:9], v[168:169]
	v_pk_fma_f32 v[30:31], v[166:167], v[6:7], v[170:171]
	v_pk_mul_f32 v[6:7], v[14:15], v[124:125] op_sel_hi:[1,0]
	v_pk_mul_f32 v[8:9], v[12:13], v[124:125] op_sel_hi:[1,0]
	v_pk_fma_f32 v[100:101], v[152:153], v[24:25], v[148:149]
	v_pk_fma_f32 v[96:97], v[156:157], v[22:23], v[160:161]
	s_waitcnt vmcnt(11)
	v_pk_fma_f32 v[22:23], v[172:173], v[8:9], v[176:177]
	v_pk_fma_f32 v[24:25], v[174:175], v[6:7], v[178:179]
	v_pk_mul_f32 v[6:7], v[18:19], v[124:125] op_sel_hi:[1,0]
	v_pk_mul_f32 v[8:9], v[120:121], v[124:125] op_sel_hi:[1,0]
	global_load_dwordx2 v[120:121], v[10:11], off offset:512
	s_waitcnt vmcnt(10)
	v_pk_fma_f32 v[18:19], v[182:183], v[6:7], v[186:187]
	v_pk_mul_f32 v[6:7], v[122:123], v[124:125] op_sel_hi:[1,0]
	v_pk_mul_f32 v[0:1], v[0:1], v[124:125] op_sel_hi:[1,0]
	s_waitcnt vmcnt(8)
	v_pk_fma_f32 v[12:13], v[190:191], v[6:7], v[194:195]
	global_load_dwordx2 v[122:123], v[26:27], off offset:1024
	global_load_dwordx2 v[124:125], v[26:27], off offset:1536
	global_load_dwordx2 v[134:135], v[20:21], off offset:512
	v_mov_b32_e32 v81, v35
	s_waitcnt vmcnt(10)
	v_and_b32_e32 v7, 0xffff0000, v126
	v_add_f32_e32 v33, 0, v7
	v_alignbit_b32 v7, v127, v126, 16
	v_and_b32_e32 v7, 0xffff0000, v7
	v_lshlrev_b32_e32 v6, 16, v126
	v_add_f32_e32 v83, 0, v7
	v_and_b32_e32 v7, 0xffff0000, v127
	v_add_f32_e32 v6, 0, v6
	v_add_f32_e32 v85, 0, v7
	v_pk_fma_f32 v[14:15], v[180:181], v[8:9], v[184:185]
	global_load_dwordx2 v[128:129], v[10:11], off offset:1024
	v_pk_fma_f32 v[0:1], v[188:189], v[0:1], v[192:193]
	s_waitcnt vmcnt(9)
	v_lshlrev_b32_e32 v7, 16, v130
	v_add_f32_e32 v87, v6, v7
	v_lshl_add_u64 v[6:7], v[16:17], 0, v[80:81]
	global_load_dwordx4 v[6:9], v[6:7], off
	v_and_b32_e32 v81, 0xffff0000, v130
	v_add_f32_e32 v33, v33, v81
	v_alignbit_b32 v81, v131, v130, 16
	v_and_b32_e32 v81, 0xffff0000, v81
	v_add_f32_e32 v81, v83, v81
	v_and_b32_e32 v83, 0xffff0000, v131
	global_load_dwordx2 v[132:133], v[116:117], off offset:2560
	global_load_dwordx2 v[126:127], v[116:117], off offset:3072
	global_load_dwordx2 v[130:131], v[116:117], off offset:3584
	global_load_dwordx2 v[146:147], v[116:117], off offset:1024
	v_add_f32_e32 v83, v85, v83
	s_waitcnt vmcnt(13)
	v_lshlrev_b32_e32 v85, 16, v196
	v_add_f32_e32 v85, v87, v85
	v_and_b32_e32 v87, 0xffff0000, v196
	v_add_f32_e32 v33, v33, v87
	v_alignbit_b32 v87, v197, v196, 16
	v_and_b32_e32 v87, 0xffff0000, v87
	v_add_f32_e32 v81, v81, v87
	v_and_b32_e32 v87, 0xffff0000, v197
	v_add_f32_e32 v83, v83, v87
	v_add_u32_e32 v32, s8, v32
	s_waitcnt vmcnt(12)
	v_lshlrev_b32_e32 v87, 16, v112
	v_add_f32_e32 v144, v85, v87
	v_and_b32_e32 v85, 0xffff0000, v112
	v_add_f32_e32 v145, v33, v85
	v_alignbit_b32 v33, v113, v112, 16
	v_and_b32_e32 v33, 0xffff0000, v33
	v_add_f32_e32 v112, v81, v33
	v_and_b32_e32 v33, 0xffff0000, v113
	v_add_f32_e32 v113, v83, v33
	v_lshlrev_b32_e32 v33, 16, v114
	v_add_f32_e32 v33, 0, v33
	v_and_b32_e32 v81, 0xffff0000, v114
	v_add_f32_e32 v81, 0, v81
	v_alignbit_b32 v83, v115, v114, 16
	v_and_b32_e32 v83, 0xffff0000, v83
	s_waitcnt vmcnt(11)
	v_lshlrev_b32_e32 v87, 16, v118
	v_add_f32_e32 v33, v33, v87
	s_waitcnt vmcnt(10)
	v_pk_add_f32 v[4:5], v[4:5], 1.0 op_sel_hi:[1,0]
	v_pk_add_f32 v[2:3], v[2:3], 1.0 op_sel_hi:[1,0]
	v_and_b32_e32 v87, 0xffff0000, v118
	v_pk_mul_f32 v[144:145], v[2:3], v[144:145]
	v_pk_mul_f32 v[2:3], v[4:5], v[112:113]
	v_and_b32_e32 v85, 0xffff0000, v115
	global_load_dwordx2 v[112:113], v[116:117], off offset:1536
	global_load_dwordx2 v[114:115], v[116:117], off offset:2048
	v_add_f32_e32 v81, v81, v87
	global_load_dwordx2 v[116:117], v[20:21], off offset:1024
	v_alignbit_b32 v87, v119, v118, 16
	v_add_f32_e32 v83, 0, v83
	v_and_b32_e32 v87, 0xffff0000, v87
	v_add_f32_e32 v85, 0, v85
	v_add_f32_e32 v87, v83, v87
	v_and_b32_e32 v83, 0xffff0000, v119
	v_add_f32_e32 v85, v85, v83
	v_mov_b32_e32 v83, v35
	v_pk_fma_f32 v[4:5], v[108:109], s[6:7], v[144:145] op_sel_hi:[1,0,1]
	v_lshl_add_u64 v[108:109], v[16:17], 0, v[82:83]
	v_pk_fma_f32 v[2:3], v[110:111], s[6:7], v[2:3] op_sel_hi:[1,0,1]
	global_load_dwordx4 v[108:111], v[108:109], off
	s_waitcnt vmcnt(13)
	v_and_b32_e32 v83, 0xffff0000, v120
	v_add_f32_e32 v81, v81, v83
	v_alignbit_b32 v83, v121, v120, 16
	v_and_b32_e32 v83, 0xffff0000, v83
	v_lshlrev_b32_e32 v89, 16, v120
	v_add_f32_e32 v83, v87, v83
	v_and_b32_e32 v87, 0xffff0000, v121
	v_add_f32_e32 v33, v33, v89
	v_add_f32_e32 v85, v85, v87
	s_waitcnt vmcnt(10)
	v_lshlrev_b32_e32 v87, 16, v134
	v_add_f32_e32 v144, v33, v87
	v_and_b32_e32 v33, 0xffff0000, v134
	v_add_f32_e32 v145, v81, v33
	v_alignbit_b32 v33, v135, v134, 16
	v_and_b32_e32 v33, 0xffff0000, v33
	v_add_f32_e32 v134, v83, v33
	v_and_b32_e32 v33, 0xffff0000, v135
	v_add_f32_e32 v135, v85, v33
	global_load_dwordx2 v[118:119], v[20:21], off offset:1536
	global_load_dwordx2 v[120:121], v[20:21], off offset:2048
	s_waitcnt vmcnt(10)
	v_pk_add_f32 v[6:7], v[6:7], 1.0 op_sel_hi:[1,0]
	v_pk_add_f32 v[8:9], v[8:9], 1.0 op_sel_hi:[1,0]
	v_pk_mul_f32 v[144:145], v[6:7], v[144:145]
	v_pk_mul_f32 v[6:7], v[8:9], v[134:135]
	v_pk_fma_f32 v[8:9], v[104:105], s[6:7], v[144:145] op_sel_hi:[1,0,1]
	global_load_dwordx2 v[144:145], v[10:11], off offset:1536
	v_pk_fma_f32 v[6:7], v[106:107], s[6:7], v[6:7] op_sel_hi:[1,0,1]
	v_mov_b32_e32 v104, v4
	v_mov_b32_e32 v105, v8
	v_mov_b32_e32 v106, v5
	v_mov_b32_e32 v107, v9
	v_pk_add_f32 v[104:105], v[104:105], v[106:107]
	v_mov_b32_e32 v106, v2
	v_mov_b32_e32 v107, v6
	v_mov_b32_e32 v134, v3
	v_mov_b32_e32 v135, v7
	v_pk_add_f32 v[106:107], v[106:107], v[134:135]
	v_and_b32_e32 v85, 0xffff0000, v123
	v_pk_add_f32 v[104:105], v[104:105], v[106:107]
	v_add_f32_e32 v87, 0, v85
	v_add_f32_e32 v33, 0, v104
	v_add_f32_e32 v134, v33, v105
	v_lshlrev_b32_e32 v33, 16, v122
	v_add_f32_e32 v33, 0, v33
	s_waitcnt vmcnt(7)
	v_lshlrev_b32_e32 v85, 16, v146
	v_and_b32_e32 v81, 0xffff0000, v122
	v_alignbit_b32 v83, v123, v122, 16
	v_add_f32_e32 v33, v33, v85
	v_mov_b32_e32 v85, v35
	global_load_dwordx2 v[122:123], v[26:27], off offset:2048
	v_lshl_add_u64 v[104:105], v[16:17], 0, v[84:85]
	global_load_dwordx4 v[104:107], v[104:105], off
	v_and_b32_e32 v83, 0xffff0000, v83
	v_alignbit_b32 v85, v147, v146, 16
	v_add_f32_e32 v83, 0, v83
	v_and_b32_e32 v85, 0xffff0000, v85
	v_add_f32_e32 v83, v83, v85
	v_and_b32_e32 v85, 0xffff0000, v147
	v_add_f32_e32 v81, 0, v81
	v_and_b32_e32 v89, 0xffff0000, v146
	v_add_f32_e32 v85, v87, v85
	v_lshlrev_b32_e32 v87, 16, v128
	v_add_f32_e32 v81, v81, v89
	v_add_f32_e32 v33, v33, v87
	v_and_b32_e32 v87, 0xffff0000, v128
	v_add_f32_e32 v81, v81, v87
	v_alignbit_b32 v87, v129, v128, 16
	v_and_b32_e32 v87, 0xffff0000, v87
	v_add_f32_e32 v83, v83, v87
	v_and_b32_e32 v87, 0xffff0000, v129
	v_add_f32_e32 v85, v85, v87
	s_waitcnt vmcnt(6)
	v_lshlrev_b32_e32 v87, 16, v116
	v_add_f32_e32 v128, v33, v87
	v_and_b32_e32 v33, 0xffff0000, v116
	v_add_f32_e32 v129, v81, v33
	v_alignbit_b32 v33, v117, v116, 16
	v_and_b32_e32 v33, 0xffff0000, v33
	v_add_f32_e32 v116, v83, v33
	v_and_b32_e32 v33, 0xffff0000, v117
	v_add_f32_e32 v117, v85, v33
	s_waitcnt vmcnt(5)
	v_pk_add_f32 v[110:111], v[110:111], 1.0 op_sel_hi:[1,0]
	v_pk_add_f32 v[108:109], v[108:109], 1.0 op_sel_hi:[1,0]
	v_pk_mul_f32 v[110:111], v[110:111], v[116:117]
	global_load_dwordx2 v[116:117], v[10:11], off offset:2048
	v_pk_mul_f32 v[108:109], v[108:109], v[128:129]
	v_pk_fma_f32 v[102:103], v[102:103], s[6:7], v[110:111] op_sel_hi:[1,0,1]
	v_pk_fma_f32 v[100:101], v[100:101], s[6:7], v[108:109] op_sel_hi:[1,0,1]
	v_mov_b32_e32 v111, v103
	v_pk_mov_b32 v[108:109], v[100:101], v[102:103] op_sel:[1,0]
	v_mov_b32_e32 v110, v100
	v_pk_add_f32 v[108:109], v[108:109], v[110:111]
	v_mov_b32_e32 v87, v35
	v_pk_add_f32 v[128:129], v[108:109], v[108:109] op_sel:[0,1] op_sel_hi:[1,0]
	v_lshl_add_u64 v[108:109], v[16:17], 0, v[86:87]
	global_load_dwordx4 v[108:111], v[108:109], off
	v_lshlrev_b32_e32 v33, 16, v124
	v_add_f32_e32 v33, 0, v33
	v_and_b32_e32 v81, 0xffff0000, v124
	v_lshlrev_b32_e32 v89, 16, v112
	v_add_f32_e32 v81, 0, v81
	v_alignbit_b32 v83, v125, v124, 16
	v_add_f32_e32 v33, v33, v89
	v_and_b32_e32 v89, 0xffff0000, v112
	v_and_b32_e32 v83, 0xffff0000, v83
	v_add_f32_e32 v81, v81, v89
	v_alignbit_b32 v89, v113, v112, 16
	v_add_f32_e32 v83, 0, v83
	v_and_b32_e32 v89, 0xffff0000, v89
	v_and_b32_e32 v85, 0xffff0000, v125
	v_add_f32_e32 v83, v83, v89
	v_and_b32_e32 v89, 0xffff0000, v113
	global_load_dwordx2 v[112:113], v[10:11], off offset:2560
	global_load_dwordx2 v[124:125], v[10:11], off offset:3072
	global_load_dwordx2 v[146:147], v[26:27], off offset:2560
	v_add_f32_e32 v85, 0, v85
	v_add_f32_e32 v85, v85, v89
	s_waitcnt vmcnt(7)
	v_lshlrev_b32_e32 v89, 16, v144
	v_add_f32_e32 v33, v33, v89
	v_and_b32_e32 v89, 0xffff0000, v144
	v_add_f32_e32 v81, v81, v89
	v_alignbit_b32 v89, v145, v144, 16
	v_and_b32_e32 v89, 0xffff0000, v89
	v_add_f32_e32 v83, v83, v89
	v_and_b32_e32 v89, 0xffff0000, v145
	v_add_f32_e32 v85, v85, v89
	v_lshlrev_b32_e32 v89, 16, v118
	v_add_f32_e32 v144, v33, v89
	v_and_b32_e32 v33, 0xffff0000, v118
	v_add_f32_e32 v145, v81, v33
	v_alignbit_b32 v33, v119, v118, 16
	v_and_b32_e32 v33, 0xffff0000, v33
	global_load_dwordx2 v[148:149], v[26:27], off offset:3072
	global_load_dwordx2 v[150:151], v[26:27], off offset:3584
	s_waitcnt vmcnt(8)
	v_lshlrev_b32_e32 v26, 16, v122
	v_add_f32_e32 v118, v83, v33
	v_and_b32_e32 v33, 0xffff0000, v119
	v_add_f32_e32 v26, 0, v26
	v_and_b32_e32 v27, 0xffff0000, v122
	global_load_dwordx2 v[152:153], v[20:21], off offset:2560
	v_lshlrev_b32_e32 v83, 16, v114
	v_add_f32_e32 v119, v85, v33
	s_waitcnt vmcnt(8)
	v_pk_add_f32 v[106:107], v[106:107], 1.0 op_sel_hi:[1,0]
	v_pk_add_f32 v[104:105], v[104:105], 1.0 op_sel_hi:[1,0]
	v_add_f32_e32 v27, 0, v27
	v_add_f32_e32 v83, v26, v83
	v_and_b32_e32 v26, 0xffff0000, v114
	v_mov_b32_e32 v89, v35
	v_pk_mul_f32 v[104:105], v[104:105], v[144:145]
	v_pk_mul_f32 v[106:107], v[106:107], v[118:119]
	v_add_f32_e32 v85, v27, v26
	v_lshl_add_u64 v[26:27], v[16:17], 0, v[88:89]
	v_pk_fma_f32 v[98:99], v[98:99], s[6:7], v[106:107] op_sel_hi:[1,0,1]
	v_pk_fma_f32 v[96:97], v[96:97], s[6:7], v[104:105] op_sel_hi:[1,0,1]
	global_load_dwordx4 v[104:107], v[26:27], off
	v_alignbit_b32 v33, v123, v122, 16
	v_and_b32_e32 v33, 0xffff0000, v33
	v_alignbit_b32 v26, v115, v114, 16
	v_add_f32_e32 v33, 0, v33
	v_and_b32_e32 v26, 0xffff0000, v26
	v_add_f32_e32 v26, v33, v26
	v_and_b32_e32 v81, 0xffff0000, v123
	v_add_f32_e32 v81, 0, v81
	v_and_b32_e32 v27, 0xffff0000, v115
	v_add_f32_e32 v27, v81, v27
	v_add_f32_e32 v118, v96, v97
	s_waitcnt vmcnt(8)
	v_lshlrev_b32_e32 v33, 16, v116
	v_add_f32_e32 v33, v83, v33
	v_alignbit_b32 v83, v117, v116, 16
	v_and_b32_e32 v83, 0xffff0000, v83
	v_and_b32_e32 v81, 0xffff0000, v116
	v_add_f32_e32 v83, v26, v83
	v_and_b32_e32 v26, 0xffff0000, v117
	v_add_f32_e32 v81, v85, v81
	v_add_f32_e32 v85, v27, v26
	v_lshlrev_b32_e32 v26, 16, v120
	v_add_f32_e32 v26, v33, v26
	v_alignbit_b32 v33, v121, v120, 16
	v_and_b32_e32 v33, 0xffff0000, v33
	v_and_b32_e32 v27, 0xffff0000, v120
	v_add_f32_e32 v114, v83, v33
	v_and_b32_e32 v33, 0xffff0000, v121
	v_add_f32_e32 v27, v81, v27
	v_add_f32_e32 v115, v85, v33
	s_waitcnt vmcnt(7)
	v_pk_add_f32 v[110:111], v[110:111], 1.0 op_sel_hi:[1,0]
	v_pk_add_f32 v[108:109], v[108:109], 1.0 op_sel_hi:[1,0]
	v_add_f32_e32 v144, v98, v99
	v_pk_mul_f32 v[26:27], v[108:109], v[26:27]
	v_pk_mul_f32 v[108:109], v[110:111], v[114:115]
	v_pk_fma_f32 v[26:27], v[28:29], s[6:7], v[26:27] op_sel_hi:[1,0,1]
	v_pk_fma_f32 v[30:31], v[30:31], s[6:7], v[108:109] op_sel_hi:[1,0,1]
	v_mov_b32_e32 v135, v26
	v_mov_b32_e32 v129, v27
	v_mov_b32_e32 v119, v30
	v_mov_b32_e32 v145, v31
	v_pk_add_f32 v[28:29], v[134:135], v[128:129]
	v_pk_add_f32 v[108:109], v[118:119], v[144:145]
	global_load_dwordx2 v[114:115], v[20:21], off offset:3072
	v_pk_add_f32 v[28:29], v[28:29], v[108:109]
	s_waitcnt vmcnt(5)
	v_and_b32_e32 v33, 0xffff0000, v146
	v_pk_add_f32 v[28:29], v[28:29], v[28:29] op_sel:[0,1] op_sel_hi:[1,0]
	v_lshl_add_u64 v[108:109], v[16:17], 0, v[90:91]
	v_lshlrev_b32_e32 v29, 16, v146
	v_add_f32_e32 v29, 0, v29
	v_lshlrev_b32_e32 v85, 16, v132
	v_add_f32_e32 v33, 0, v33
	v_alignbit_b32 v81, v147, v146, 16
	global_load_dwordx4 v[108:111], v[108:109], off
	v_add_f32_e32 v29, v29, v85
	v_and_b32_e32 v85, 0xffff0000, v132
	v_and_b32_e32 v81, 0xffff0000, v81
	v_add_f32_e32 v33, v33, v85
	v_alignbit_b32 v85, v133, v132, 16
	v_add_f32_e32 v81, 0, v81
	v_and_b32_e32 v83, 0xffff0000, v147
	v_and_b32_e32 v85, 0xffff0000, v85
	v_add_f32_e32 v83, 0, v83
	v_add_f32_e32 v81, v81, v85
	v_and_b32_e32 v85, 0xffff0000, v133
	v_add_f32_e32 v83, v83, v85
	v_lshlrev_b32_e32 v85, 16, v112
	v_add_f32_e32 v29, v29, v85
	v_and_b32_e32 v85, 0xffff0000, v112
	v_add_f32_e32 v33, v33, v85
	v_alignbit_b32 v85, v113, v112, 16
	v_and_b32_e32 v85, 0xffff0000, v85
	v_add_f32_e32 v81, v81, v85
	v_and_b32_e32 v85, 0xffff0000, v113
	global_load_dwordx2 v[112:113], v[20:21], off offset:3584
	global_load_dwordx2 v[116:117], v[10:11], off offset:3584
	s_waitcnt vmcnt(5)
	v_lshlrev_b32_e32 v20, 16, v152
	v_add_f32_e32 v20, v29, v20
	v_alignbit_b32 v29, v153, v152, 16
	v_add_f32_e32 v83, v83, v85
	v_and_b32_e32 v21, 0xffff0000, v152
	v_and_b32_e32 v29, 0xffff0000, v29
	v_and_b32_e32 v11, 0xffff0000, v153
	v_add_f32_e32 v21, v33, v21
	v_add_f32_e32 v10, v81, v29
	v_add_f32_e32 v11, v83, v11
	s_waitcnt vmcnt(4)
	v_pk_add_f32 v[106:107], v[106:107], 1.0 op_sel_hi:[1,0]
	v_pk_add_f32 v[104:105], v[104:105], 1.0 op_sel_hi:[1,0]
	v_pk_mul_f32 v[10:11], v[106:107], v[10:11]
	v_pk_mul_f32 v[104:105], v[104:105], v[20:21]
	v_pk_fma_f32 v[20:21], v[24:25], s[6:7], v[10:11] op_sel_hi:[1,0,1]
	v_pk_fma_f32 v[10:11], v[22:23], s[6:7], v[104:105] op_sel_hi:[1,0,1]
	v_mov_b32_e32 v25, v21
	v_pk_mov_b32 v[22:23], v[10:11], v[20:21] op_sel:[1,0]
	v_mov_b32_e32 v24, v10
	v_pk_add_f32 v[22:23], v[22:23], v[24:25]
	v_lshl_add_u64 v[16:17], v[16:17], 0, v[92:93]
	v_pk_add_f32 v[104:105], v[22:23], v[22:23] op_sel:[0,1] op_sel_hi:[1,0]
	global_load_dwordx4 v[22:25], v[16:17], off
	v_lshlrev_b32_e32 v29, 16, v148
	v_add_f32_e32 v16, 0, v29
	v_and_b32_e32 v17, 0xffff0000, v148
	v_lshlrev_b32_e32 v81, 16, v126
	v_add_f32_e32 v17, 0, v17
	v_alignbit_b32 v29, v149, v148, 16
	v_add_f32_e32 v16, v16, v81
	v_and_b32_e32 v81, 0xffff0000, v126
	v_and_b32_e32 v29, 0xffff0000, v29
	v_add_f32_e32 v17, v17, v81
	v_alignbit_b32 v81, v127, v126, 16
	v_add_f32_e32 v29, 0, v29
	v_and_b32_e32 v33, 0xffff0000, v149
	v_and_b32_e32 v81, 0xffff0000, v81
	v_add_f32_e32 v33, 0, v33
	v_add_f32_e32 v29, v29, v81
	v_and_b32_e32 v81, 0xffff0000, v127
	v_add_f32_e32 v33, v33, v81
	v_lshlrev_b32_e32 v81, 16, v124
	v_add_f32_e32 v16, v16, v81
	v_and_b32_e32 v81, 0xffff0000, v124
	v_add_f32_e32 v17, v17, v81
	v_alignbit_b32 v81, v125, v124, 16
	v_and_b32_e32 v81, 0xffff0000, v81
	v_add_f32_e32 v29, v29, v81
	v_and_b32_e32 v81, 0xffff0000, v125
	v_add_f32_e32 v33, v33, v81
	s_waitcnt vmcnt(4)
	v_lshlrev_b32_e32 v81, 16, v114
	v_add_f32_e32 v16, v16, v81
	v_and_b32_e32 v81, 0xffff0000, v114
	v_add_f32_e32 v17, v17, v81
	v_alignbit_b32 v81, v115, v114, 16
	v_and_b32_e32 v81, 0xffff0000, v81
	v_add_f32_e32 v106, v29, v81
	v_and_b32_e32 v29, 0xffff0000, v115
	v_add_f32_e32 v107, v33, v29
	s_waitcnt vmcnt(3)
	v_pk_add_f32 v[110:111], v[110:111], 1.0 op_sel_hi:[1,0]
	v_pk_add_f32 v[108:109], v[108:109], 1.0 op_sel_hi:[1,0]
	v_and_b32_e32 v29, 0xffff0000, v150
	v_pk_mul_f32 v[108:109], v[108:109], v[16:17]
	v_pk_mul_f32 v[16:17], v[110:111], v[106:107]
	v_lshlrev_b32_e32 v83, 16, v130
	v_pk_fma_f32 v[16:17], v[18:19], s[6:7], v[16:17] op_sel_hi:[1,0,1]
	v_lshlrev_b32_e32 v19, 16, v150
	v_add_f32_e32 v19, 0, v19
	v_add_f32_e32 v29, 0, v29
	v_alignbit_b32 v33, v151, v150, 16
	v_add_f32_e32 v19, v19, v83
	v_and_b32_e32 v83, 0xffff0000, v130
	v_and_b32_e32 v33, 0xffff0000, v33
	v_add_f32_e32 v29, v29, v83
	v_alignbit_b32 v83, v131, v130, 16
	v_add_f32_e32 v33, 0, v33
	v_and_b32_e32 v81, 0xffff0000, v151
	v_and_b32_e32 v83, 0xffff0000, v83
	v_add_f32_e32 v81, 0, v81
	v_add_f32_e32 v33, v33, v83
	v_and_b32_e32 v83, 0xffff0000, v131
	v_add_f32_e32 v81, v81, v83
	s_waitcnt vmcnt(1)
	v_lshlrev_b32_e32 v83, 16, v116
	v_add_f32_e32 v19, v19, v83
	v_and_b32_e32 v83, 0xffff0000, v116
	v_add_f32_e32 v29, v29, v83
	v_alignbit_b32 v83, v117, v116, 16
	v_and_b32_e32 v83, 0xffff0000, v83
	v_add_f32_e32 v33, v33, v83
	v_and_b32_e32 v83, 0xffff0000, v117
	v_add_f32_e32 v81, v81, v83
	v_lshlrev_b32_e32 v83, 16, v112
	v_pk_fma_f32 v[14:15], v[14:15], s[6:7], v[108:109] op_sel_hi:[1,0,1]
	v_add_f32_e32 v108, v19, v83
	v_and_b32_e32 v19, 0xffff0000, v112
	v_add_f32_e32 v109, v29, v19
	v_alignbit_b32 v19, v113, v112, 16
	v_and_b32_e32 v19, 0xffff0000, v19
	v_add_f32_e32 v110, v33, v19
	v_and_b32_e32 v19, 0xffff0000, v113
	v_add_f32_e32 v111, v81, v19
	v_add_f32_e32 v18, v14, v15
	s_waitcnt vmcnt(0)
	v_pk_add_f32 v[24:25], v[24:25], 1.0 op_sel_hi:[1,0]
	v_pk_add_f32 v[22:23], v[22:23], 1.0 op_sel_hi:[1,0]
	v_pk_mul_f32 v[24:25], v[24:25], v[110:111]
	v_pk_mul_f32 v[22:23], v[22:23], v[108:109]
	v_pk_fma_f32 v[12:13], v[12:13], s[6:7], v[24:25] op_sel_hi:[1,0,1]
	v_pk_fma_f32 v[0:1], v[0:1], s[6:7], v[22:23] op_sel_hi:[1,0,1]
	v_add_f32_e32 v106, v16, v17
	v_mov_b32_e32 v29, v0
	v_mov_b32_e32 v105, v1
	v_mov_b32_e32 v19, v12
	v_mov_b32_e32 v107, v13
	v_pk_add_f32 v[22:23], v[28:29], v[104:105]
	v_pk_add_f32 v[18:19], v[18:19], v[106:107]
	s_nop 0
	v_pk_add_f32 v[18:19], v[22:23], v[18:19]
	s_nop 0
	v_add_f32_e32 v18, v18, v19
	ds_bpermute_b32 v19, v136, v18
	s_waitcnt lgkmcnt(0)
	v_add_f32_e32 v18, v18, v19
	ds_bpermute_b32 v19, v137, v18
	s_waitcnt lgkmcnt(0)
	v_add_f32_e32 v18, v18, v19
	ds_bpermute_b32 v19, v138, v18
	s_waitcnt lgkmcnt(0)
	v_add_f32_e32 v18, v18, v19
	ds_bpermute_b32 v19, v139, v18
	s_waitcnt lgkmcnt(0)
	v_add_f32_e32 v18, v18, v19
	ds_bpermute_b32 v19, v140, v18
	s_waitcnt lgkmcnt(0)
	v_add_f32_e32 v18, v18, v19
	ds_bpermute_b32 v19, v141, v18
	s_waitcnt lgkmcnt(0)
	v_add_f32_e32 v33, v18, v19
	v_fmamk_f32 v5, v33, 0xba000000, v5
	v_fmamk_f32 v9, v33, 0xba000000, v9
	v_fmamk_f32 v3, v33, 0xba000000, v3
	v_fmac_f32_e32 v4, 0xba000000, v33
	v_fmamk_f32 v7, v33, 0xba000000, v7
	v_fmac_f32_e32 v8, 0xba000000, v33
	v_mov_b32_e32 v22, v5
	v_mov_b32_e32 v23, v9
	v_fmac_f32_e32 v2, 0xba000000, v33
	v_fmac_f32_e32 v6, 0xba000000, v33
	v_mov_b32_e32 v18, v4
	v_mov_b32_e32 v19, v8
	v_pk_mul_f32 v[22:23], v[22:23], v[22:23]
	v_mov_b32_e32 v24, v3
	v_mov_b32_e32 v25, v7
	v_pk_fma_f32 v[18:19], v[18:19], v[18:19], v[22:23]
	v_mov_b32_e32 v22, v2
	v_mov_b32_e32 v23, v6
	v_pk_mul_f32 v[24:25], v[24:25], v[24:25]
	v_fmamk_f32 v101, v33, 0xba000000, v101
	v_pk_fma_f32 v[22:23], v[22:23], v[22:23], v[24:25]
	v_fmac_f32_e32 v100, 0xba000000, v33
	v_pk_add_f32 v[18:19], v[18:19], v[22:23]
	v_fmamk_f32 v103, v33, 0xba000000, v103
	v_fmac_f32_e32 v102, 0xba000000, v33
	v_pk_add_f32 v[18:19], v[18:19], v[18:19] op_sel_hi:[0,1]
	v_pk_mul_f32 v[22:23], v[102:103], v[102:103]
	v_pk_mul_f32 v[24:25], v[100:101], v[100:101]
	v_fmac_f32_e32 v96, 0xba000000, v33
	v_pk_mov_b32 v[28:29], v[24:25], v[22:23] op_sel:[1,0]
	v_mov_b32_e32 v25, v23
	v_fmamk_f32 v97, v33, 0xba000000, v97
	v_fmac_f32_e32 v98, 0xba000000, v33
	v_mul_f32_e32 v18, v96, v96
	v_pk_add_f32 v[22:23], v[28:29], v[24:25]
	v_fmamk_f32 v99, v33, 0xba000000, v99
	v_pk_fma_f32 v[24:25], v[96:97], v[96:97], v[18:19] op_sel_hi:[1,1,0]
	v_mul_f32_e32 v18, v98, v98
	v_pk_add_f32 v[22:23], v[22:23], v[22:23] op_sel_hi:[0,1]
	v_pk_fma_f32 v[28:29], v[98:99], v[98:99], v[18:19] op_sel_hi:[1,1,0]
	v_fmamk_f32 v31, v33, 0xba000000, v31
	v_fmac_f32_e32 v30, 0xba000000, v33
	v_fmamk_f32 v27, v33, 0xba000000, v27
	v_fmac_f32_e32 v26, 0xba000000, v33
	v_mul_f32_e32 v24, v26, v26
	v_mul_f32_e32 v28, v27, v27
	v_mul_f32_e32 v22, v30, v30
	v_mul_f32_e32 v18, v31, v31
	v_pk_add_f32 v[24:25], v[24:25], v[28:29]
	v_pk_add_f32 v[18:19], v[22:23], v[18:19]
	v_fmamk_f32 v11, v33, 0xba000000, v11
	v_fmac_f32_e32 v10, 0xba000000, v33
	v_fmamk_f32 v21, v33, 0xba000000, v21
	v_fmac_f32_e32 v20, 0xba000000, v33
	v_pk_add_f32 v[18:19], v[24:25], v[18:19]
	v_pk_mul_f32 v[22:23], v[20:21], v[20:21]
	v_pk_mul_f32 v[24:25], v[10:11], v[10:11]
	v_pk_add_f32 v[18:19], v[18:19], v[18:19] op_sel_hi:[0,1]
	v_pk_mov_b32 v[28:29], v[24:25], v[22:23] op_sel:[1,0]
	v_mov_b32_e32 v25, v23
	v_pk_add_f32 v[22:23], v[28:29], v[24:25]
	v_fmac_f32_e32 v14, 0xba000000, v33
	v_pk_add_f32 v[28:29], v[22:23], v[22:23] op_sel_hi:[0,1]
	global_load_dwordx4 v[22:25], v[58:59], off
	global_load_dwordx4 v[104:107], v[60:61], off
	v_fmamk_f32 v15, v33, 0xba000000, v15
	v_fmac_f32_e32 v16, 0xba000000, v33
	v_mul_f32_e32 v18, v14, v14
	v_fmamk_f32 v17, v33, 0xba000000, v17
	v_pk_fma_f32 v[108:109], v[14:15], v[14:15], v[18:19] op_sel_hi:[1,1,0]
	v_mul_f32_e32 v18, v16, v16
	v_pk_fma_f32 v[110:111], v[16:17], v[16:17], v[18:19] op_sel_hi:[1,1,0]
	v_fmamk_f32 v13, v33, 0xba000000, v13
	v_fmac_f32_e32 v12, 0xba000000, v33
	v_fmamk_f32 v1, v33, 0xba000000, v1
	v_fmac_f32_e32 v0, 0xba000000, v33
	v_mul_f32_e32 v108, v0, v0
	v_mul_f32_e32 v110, v1, v1
	v_mul_f32_e32 v28, v12, v12
	v_mul_f32_e32 v18, v13, v13
	v_pk_add_f32 v[108:109], v[108:109], v[110:111]
	v_pk_add_f32 v[18:19], v[28:29], v[18:19]
	s_nop 0
	v_pk_add_f32 v[18:19], v[108:109], v[18:19]
	s_nop 0
	v_add_f32_e32 v18, v18, v19
	ds_bpermute_b32 v19, v136, v18
	s_waitcnt lgkmcnt(0)
	v_add_f32_e32 v18, v18, v19
	ds_bpermute_b32 v19, v137, v18
	s_waitcnt lgkmcnt(0)
	v_add_f32_e32 v18, v18, v19
	ds_bpermute_b32 v19, v138, v18
	s_waitcnt lgkmcnt(0)
	v_add_f32_e32 v18, v18, v19
	ds_bpermute_b32 v19, v139, v18
	s_waitcnt lgkmcnt(0)
	v_add_f32_e32 v18, v18, v19
	ds_bpermute_b32 v19, v140, v18
	s_waitcnt lgkmcnt(0)
	v_add_f32_e32 v18, v18, v19
	ds_bpermute_b32 v19, v141, v18
	s_waitcnt lgkmcnt(0)
	v_add_f32_e32 v18, v18, v19
	v_fmamk_f32 v18, v18, 0x3a000000, v142
	v_mul_f32_e32 v19, 0x4f800000, v18
	v_cmp_gt_f32_e32 vcc, s10, v18
	s_nop 1
	v_cndmask_b32_e32 v18, v18, v19, vcc
	v_sqrt_f32_e32 v19, v18
	s_nop 0
	v_add_u32_e32 v28, -1, v19
	v_fma_f32 v29, -v28, v19, v18
	v_cmp_ge_f32_e64 s[0:1], 0, v29
	v_add_u32_e32 v29, 1, v19
	s_nop 0
	v_cndmask_b32_e64 v28, v19, v28, s[0:1]
	v_fma_f32 v19, -v29, v19, v18
	v_cmp_lt_f32_e64 s[0:1], 0, v19
	s_nop 1
	v_cndmask_b32_e64 v19, v28, v29, s[0:1]
	v_mul_f32_e32 v28, 0x37800000, v19
	v_cndmask_b32_e32 v19, v19, v28, vcc
	v_cmp_class_f32_e32 vcc, v18, v143
	s_nop 1
	v_cndmask_b32_e32 v18, v19, v18, vcc
	v_div_scale_f32 v19, s[0:1], v18, v18, 1.0
	v_rcp_f32_e32 v28, v19
	s_nop 0
	v_fma_f32 v29, -v19, v28, 1.0
	v_fmac_f32_e32 v28, v29, v28
	v_div_scale_f32 v29, vcc, 1.0, v18, 1.0
	v_mul_f32_e32 v33, v29, v28
	v_fma_f32 v81, -v19, v33, v29
	v_fmac_f32_e32 v33, v81, v28
	v_fma_f32 v19, -v19, v33, v29
	v_div_fmas_f32 v19, v19, v28, v33
	v_div_fixup_f32 v18, v19, v18, 1.0
	v_pk_mul_f32 v[28:29], v[4:5], v[18:19] op_sel_hi:[1,0]
	v_pk_mul_f32 v[2:3], v[2:3], v[18:19] op_sel_hi:[1,0]
	v_pk_mul_f32 v[6:7], v[6:7], v[18:19] op_sel_hi:[1,0]
	s_waitcnt vmcnt(0)
	v_pk_fma_f32 v[4:5], v[24:25], v[2:3], v[106:107]
	v_pk_fma_f32 v[2:3], v[22:23], v[28:29], v[104:105]
	global_load_dwordx4 v[104:107], v[76:77], off
	v_lshl_add_u64 v[28:29], s[26:27], 0, v[94:95]
	v_lshl_add_u64 v[94:95], v[28:29], 0, v[34:35]
	global_store_dwordx4 v[94:95], v[2:5], off
	v_pk_mul_f32 v[8:9], v[8:9], v[18:19] op_sel_hi:[1,0]
	v_pk_mul_f32 v[20:21], v[20:21], v[18:19] op_sel_hi:[1,0]
	v_pk_mul_f32 v[10:11], v[10:11], v[18:19] op_sel_hi:[1,0]
	v_pk_mul_f32 v[14:15], v[14:15], v[18:19] op_sel_hi:[1,0]
	v_cmp_lt_i32_e32 vcc, s12, v32
	v_pk_mul_f32 v[12:13], v[12:13], v[18:19] op_sel_hi:[1,0]
	v_pk_mul_f32 v[0:1], v[0:1], v[18:19] op_sel_hi:[1,0]
	s_or_b64 s[2:3], vcc, s[2:3]
	v_pk_fma_f32 v[2:3], v[198:199], v[8:9], v[202:203]
	v_pk_fma_f32 v[4:5], v[200:201], v[6:7], v[204:205]
	global_store_dwordx4 v[94:95], v[2:5], off offset:1024
	v_pk_mul_f32 v[22:23], v[102:103], v[18:19] op_sel_hi:[1,0]
	v_pk_mul_f32 v[24:25], v[100:101], v[18:19] op_sel_hi:[1,0]
	v_pk_fma_f32 v[4:5], v[208:209], v[22:23], v[212:213]
	v_pk_fma_f32 v[2:3], v[206:207], v[24:25], v[210:211]
	global_store_dwordx4 v[94:95], v[2:5], off offset:2048
	v_pk_mul_f32 v[22:23], v[98:99], v[18:19] op_sel_hi:[1,0]
	v_pk_mul_f32 v[24:25], v[96:97], v[18:19] op_sel_hi:[1,0]
	v_pk_fma_f32 v[4:5], v[216:217], v[22:23], v[220:221]
	v_pk_fma_f32 v[2:3], v[214:215], v[24:25], v[218:219]
	global_store_dwordx4 v[94:95], v[2:5], off offset:3072
	v_pk_mul_f32 v[22:23], v[30:31], v[18:19] op_sel_hi:[1,0]
	v_pk_mul_f32 v[24:25], v[26:27], v[18:19] op_sel_hi:[1,0]
	v_pk_fma_f32 v[4:5], v[226:227], v[22:23], v[230:231]
	v_pk_fma_f32 v[2:3], v[224:225], v[24:25], v[228:229]
	v_lshl_add_u64 v[6:7], v[28:29], 0, v[86:87]
	global_store_dwordx4 v[6:7], v[2:5], off
	s_nop 1
	v_pk_fma_f32 v[2:3], v[232:233], v[10:11], v[236:237]
	v_pk_fma_f32 v[4:5], v[234:235], v[20:21], v[238:239]
	v_lshl_add_u64 v[6:7], v[28:29], 0, v[88:89]
	global_store_dwordx4 v[6:7], v[2:5], off
	v_pk_mul_f32 v[10:11], v[16:17], v[18:19] op_sel_hi:[1,0]
	s_nop 0
	v_pk_fma_f32 v[2:3], v[240:241], v[14:15], v[244:245]
	v_pk_fma_f32 v[4:5], v[242:243], v[10:11], v[246:247]
	v_lshl_add_u64 v[6:7], v[28:29], 0, v[90:91]
	global_store_dwordx4 v[6:7], v[2:5], off
	v_lshl_add_u64 v[10:11], v[28:29], 0, v[92:93]
	s_waitcnt vmcnt(7)
	v_pk_fma_f32 v[0:1], v[248:249], v[0:1], v[104:105]
	v_pk_fma_f32 v[2:3], v[250:251], v[12:13], v[106:107]
	global_store_dwordx4 v[10:11], v[0:3], off
	s_andn2_b64 exec, exec, s[2:3]
	s_cbranch_execnz .LBB0_1397
